# prep phase adaLN tasks: the two conditioning loads issued first, then the 64 weight-row loads, one counted wait; silu stage and both barriers now run while the weight rows are in flight
# speedup vs baseline: 1.0133x; 1.0036x over previous
; __device__ void adaln_partial_task(KParams& p, int task, float* sm) {
;     ...
;   const int col = cb * 256 + tid;
;   float a0 = 0, a1 = 0, a2 = 0, a3 = 0, a4 = 0;
;   const float* wp = p.w_mod + (size_t)(ks * 64) * NMOD + col;
;   {
;     float wv[64];
; #pragma unroll
;     for (int kk = 0; kk < 64; ++kk) wv[kk] = __builtin_nontemporal_load(wp + (size_t)kk * NMOD);
.LBB0_15:
	s_or_b64 exec, exec, s[18:19]
	s_mul_i32 s18, s91, 48
	s_sub_i32 s18, s90, s18
	v_lshl_or_b32 v2, s18, 8, v0
	s_mul_hi_i32 s19, s92, 0xc000
	s_mul_i32 s92, s92, 0xc000
	s_add_u32 s18, s10, s92
	v_ashrrev_i32_e32 v3, 31, v2
	s_addc_u32 s19, s11, s19
	v_lshlrev_b64 v[2:3], 2, v[2:3]
	v_lshl_add_u64 v[4:5], s[18:19], 0, v[2:3]
	v_add_co_u32_e32 v8, vcc, s22, v4
	s_waitcnt lgkmcnt(0)
	s_nop 0
	v_addc_co_u32_e32 v9, vcc, 0, v5, vcc
	v_add_co_u32_e32 v10, vcc, s23, v4
	s_nop 0
	s_nop 0
	v_addc_co_u32_e32 v11, vcc, 0, v5, vcc
	v_add_co_u32_e32 v12, vcc, s24, v4
	s_nop 1
	v_addc_co_u32_e32 v13, vcc, 0, v5, vcc
	v_add_co_u32_e32 v14, vcc, s25, v4
	s_mul_i32 s18, s91, 5
	s_nop 0
	v_addc_co_u32_e32 v15, vcc, 0, v5, vcc
	v_add_co_u32_e32 v16, vcc, s26, v4
	s_mul_i32 s91, s91, 0x3c000
	s_nop 0
	v_addc_co_u32_e32 v17, vcc, 0, v5, vcc
	v_add_co_u32_e32 v18, vcc, s27, v4
	s_mul_hi_i32 s19, s18, 0xc000
	s_nop 0
	v_addc_co_u32_e32 v19, vcc, 0, v5, vcc
	v_add_co_u32_e32 v20, vcc, s28, v4
	s_add_u32 s18, s16, s91
	s_nop 0
	v_addc_co_u32_e32 v21, vcc, 0, v5, vcc
	global_load_dword v114, v[4:5], off nt
	global_load_dword v115, v[8:9], off nt
	global_load_dword v116, v[10:11], off nt
	global_load_dword v117, v[12:13], off nt
	global_load_dword v118, v[14:15], off nt
	global_load_dword v119, v[16:17], off nt
	global_load_dword v120, v[18:19], off nt
	global_load_dword v121, v[20:21], off nt
	v_add_co_u32_e32 v8, vcc, s29, v4
	s_addc_u32 s19, s17, s19
	s_nop 0
	v_addc_co_u32_e32 v9, vcc, 0, v5, vcc
	v_add_co_u32_e32 v10, vcc, s30, v4
	v_lshl_add_u64 v[2:3], s[18:19], 0, v[2:3]
	s_nop 0
	v_addc_co_u32_e32 v11, vcc, 0, v5, vcc
	v_add_co_u32_e32 v12, vcc, s31, v4
	s_add_i32 s90, s90, s100
	s_nop 0
	v_addc_co_u32_e32 v13, vcc, 0, v5, vcc
	v_add_co_u32_e32 v14, vcc, s35, v4
	s_cmp_gt_i32 s90, s101
	s_nop 0
	v_addc_co_u32_e32 v15, vcc, 0, v5, vcc
	v_add_co_u32_e32 v16, vcc, s36, v4
	s_nop 1
	v_addc_co_u32_e32 v17, vcc, 0, v5, vcc
	v_add_co_u32_e32 v18, vcc, s37, v4
	s_nop 1
	v_addc_co_u32_e32 v19, vcc, 0, v5, vcc
	v_add_co_u32_e32 v20, vcc, s38, v4
	s_nop 1
	v_addc_co_u32_e32 v21, vcc, 0, v5, vcc
	v_add_co_u32_e32 v22, vcc, s39, v4
	s_nop 1
	v_addc_co_u32_e32 v23, vcc, 0, v5, vcc
	global_load_dword v65, v[8:9], off nt
	global_load_dword v64, v[10:11], off nt
	global_load_dword v63, v[12:13], off nt
	global_load_dword v62, v[14:15], off nt
	global_load_dword v61, v[16:17], off nt
	global_load_dword v60, v[18:19], off nt
	global_load_dword v59, v[20:21], off nt
	global_load_dword v58, v[22:23], off nt
	v_add_co_u32_e32 v8, vcc, s40, v4
	s_nop 1
	v_addc_co_u32_e32 v9, vcc, 0, v5, vcc
	v_add_co_u32_e32 v10, vcc, s41, v4
	s_nop 1
	v_addc_co_u32_e32 v11, vcc, 0, v5, vcc
	v_add_co_u32_e32 v12, vcc, s42, v4
	s_nop 1
	v_addc_co_u32_e32 v13, vcc, 0, v5, vcc
	v_add_co_u32_e32 v14, vcc, s43, v4
	s_nop 1
	v_addc_co_u32_e32 v15, vcc, 0, v5, vcc
	v_add_co_u32_e32 v16, vcc, s46, v4
	s_nop 1
	v_addc_co_u32_e32 v17, vcc, 0, v5, vcc
	v_add_co_u32_e32 v18, vcc, s47, v4
	s_nop 1
	v_addc_co_u32_e32 v19, vcc, 0, v5, vcc
	v_add_co_u32_e32 v20, vcc, s48, v4
	s_nop 1
	v_addc_co_u32_e32 v21, vcc, 0, v5, vcc
	v_add_co_u32_e32 v22, vcc, s49, v4
	s_nop 1
	v_addc_co_u32_e32 v23, vcc, 0, v5, vcc
	global_load_dword v57, v[8:9], off nt
	global_load_dword v56, v[10:11], off nt
	global_load_dword v55, v[12:13], off nt
	global_load_dword v54, v[14:15], off nt
	global_load_dword v53, v[16:17], off nt
	global_load_dword v52, v[18:19], off nt
	global_load_dword v51, v[20:21], off nt
	global_load_dword v50, v[22:23], off nt
	v_add_co_u32_e32 v8, vcc, s50, v4
	s_nop 1
	v_addc_co_u32_e32 v9, vcc, 0, v5, vcc
	v_add_co_u32_e32 v10, vcc, s51, v4
	s_nop 1
	v_addc_co_u32_e32 v11, vcc, 0, v5, vcc
	v_add_co_u32_e32 v12, vcc, s52, v4
	s_nop 1
	v_addc_co_u32_e32 v13, vcc, 0, v5, vcc
	v_add_co_u32_e32 v14, vcc, s53, v4
	s_nop 1
	v_addc_co_u32_e32 v15, vcc, 0, v5, vcc
	v_add_co_u32_e32 v16, vcc, s54, v4
	s_nop 1
	v_addc_co_u32_e32 v17, vcc, 0, v5, vcc
	v_add_co_u32_e32 v18, vcc, s55, v4
	s_nop 1
	v_addc_co_u32_e32 v19, vcc, 0, v5, vcc
	v_add_co_u32_e32 v20, vcc, s56, v4
	s_nop 1
	v_addc_co_u32_e32 v21, vcc, 0, v5, vcc
	v_add_co_u32_e32 v22, vcc, s57, v4
	s_nop 1
	v_addc_co_u32_e32 v23, vcc, 0, v5, vcc
	global_load_dword v49, v[8:9], off nt
	global_load_dword v48, v[10:11], off nt
	global_load_dword v47, v[12:13], off nt
	global_load_dword v46, v[14:15], off nt
	global_load_dword v45, v[16:17], off nt
	global_load_dword v44, v[18:19], off nt
	global_load_dword v43, v[20:21], off nt
	global_load_dword v42, v[22:23], off nt
	v_add_co_u32_e32 v8, vcc, s58, v4
	s_nop 1
	v_addc_co_u32_e32 v9, vcc, 0, v5, vcc
	v_add_co_u32_e32 v10, vcc, s59, v4
	s_nop 1
	v_addc_co_u32_e32 v11, vcc, 0, v5, vcc
	v_add_co_u32_e32 v12, vcc, s60, v4
	s_nop 1
	v_addc_co_u32_e32 v13, vcc, 0, v5, vcc
	v_add_co_u32_e32 v14, vcc, s61, v4
	s_nop 1
	v_addc_co_u32_e32 v15, vcc, 0, v5, vcc
	v_add_co_u32_e32 v16, vcc, s62, v4
	s_nop 1
	v_addc_co_u32_e32 v17, vcc, 0, v5, vcc
	v_add_co_u32_e32 v18, vcc, s63, v4
	s_nop 1
	v_addc_co_u32_e32 v19, vcc, 0, v5, vcc
	v_add_co_u32_e32 v20, vcc, s64, v4
	s_nop 1
	v_addc_co_u32_e32 v21, vcc, 0, v5, vcc
	v_add_co_u32_e32 v22, vcc, s65, v4
	s_nop 1
	v_addc_co_u32_e32 v23, vcc, 0, v5, vcc
	global_load_dword v41, v[8:9], off nt
	global_load_dword v40, v[10:11], off nt
	global_load_dword v39, v[12:13], off nt
	global_load_dword v38, v[14:15], off nt
	global_load_dword v37, v[16:17], off nt
	global_load_dword v36, v[18:19], off nt
	global_load_dword v35, v[20:21], off nt
	global_load_dword v34, v[22:23], off nt
	v_add_co_u32_e32 v8, vcc, s66, v4
	s_nop 1
	v_addc_co_u32_e32 v9, vcc, 0, v5, vcc
	v_add_co_u32_e32 v10, vcc, s67, v4
; __device__ __forceinline__ float silu_f(float v) { return v / (1.f + __expf(-v)); }
; __device__ void adaln_partial_task(KParams& p, int task, float* sm) {
;     ...
;   for (int i = tid; i < 5 * 64; i += NTHREADS) {
;     int r = i >> 6, kk = i & 63;
;     int k = ks * 64 + kk;
;     float cv = (r < 4) ? p.c[r * D + k] : p.c_ctx[k];
;     sc[i] = silu_f(cv);
;   }
;   __syncthreads();
;   const int col = cb * 256 + tid;
;   float a0 = 0, a1 = 0, a2 = 0, a3 = 0, a4 = 0;
;   const float* wp = p.w_mod + (size_t)(ks * 64) * NMOD + col;
;   {
;     float wv[64];
; #pragma unroll
;     for (int kk = 0; kk < 64; ++kk) wv[kk] = __builtin_nontemporal_load(wp + (size_t)kk * NMOD);
; #pragma unroll
;     for (int k = 0; k < 64; ++k) {
;       a0 += sc[k] * wv[k]; a1 += sc[64 + k] * wv[k]; a2 += sc[128 + k] * wv[k]; a3 += sc[192 + k] * wv[k]; a4 += sc[256 + k] * wv[k];
	s_nop 1
	v_addc_co_u32_e32 v11, vcc, 0, v5, vcc
	v_add_co_u32_e32 v12, vcc, s68, v4
	s_nop 1
	v_addc_co_u32_e32 v13, vcc, 0, v5, vcc
	v_add_co_u32_e32 v14, vcc, s69, v4
	s_nop 1
	v_addc_co_u32_e32 v15, vcc, 0, v5, vcc
	v_add_co_u32_e32 v16, vcc, s70, v4
	s_nop 1
	v_addc_co_u32_e32 v17, vcc, 0, v5, vcc
	v_add_co_u32_e32 v18, vcc, s71, v4
	s_nop 1
	v_addc_co_u32_e32 v19, vcc, 0, v5, vcc
	v_add_co_u32_e32 v20, vcc, s72, v4
	s_nop 1
	v_addc_co_u32_e32 v21, vcc, 0, v5, vcc
	v_add_co_u32_e32 v22, vcc, s73, v4
	s_nop 1
	v_addc_co_u32_e32 v23, vcc, 0, v5, vcc
	global_load_dword v33, v[8:9], off nt
	global_load_dword v32, v[10:11], off nt
	global_load_dword v31, v[12:13], off nt
	global_load_dword v30, v[14:15], off nt
	global_load_dword v29, v[16:17], off nt
	global_load_dword v28, v[18:19], off nt
	global_load_dword v27, v[20:21], off nt
	global_load_dword v26, v[22:23], off nt
	v_add_co_u32_e32 v8, vcc, s74, v4
	s_nop 1
	v_addc_co_u32_e32 v9, vcc, 0, v5, vcc
	v_add_co_u32_e32 v10, vcc, s75, v4
	s_nop 1
	v_addc_co_u32_e32 v11, vcc, 0, v5, vcc
	v_add_co_u32_e32 v12, vcc, s76, v4
	s_nop 1
	v_addc_co_u32_e32 v13, vcc, 0, v5, vcc
	v_add_co_u32_e32 v14, vcc, s77, v4
	s_nop 1
	v_addc_co_u32_e32 v15, vcc, 0, v5, vcc
	v_add_co_u32_e32 v16, vcc, s78, v4
	s_nop 1
	v_addc_co_u32_e32 v17, vcc, 0, v5, vcc
	v_add_co_u32_e32 v18, vcc, s79, v4
	s_nop 1
	v_addc_co_u32_e32 v19, vcc, 0, v5, vcc
	v_add_co_u32_e32 v66, vcc, s80, v4
	s_nop 1
	v_addc_co_u32_e32 v67, vcc, 0, v5, vcc
	v_add_co_u32_e32 v68, vcc, s81, v4
	s_nop 1
	v_addc_co_u32_e32 v69, vcc, 0, v5, vcc
	global_load_dword v25, v[8:9], off nt
	global_load_dword v24, v[10:11], off nt
	global_load_dword v23, v[12:13], off nt
	global_load_dword v22, v[14:15], off nt
	global_load_dword v21, v[16:17], off nt
	global_load_dword v20, v[18:19], off nt
	s_nop 0
	global_load_dword v19, v[66:67], off nt
	global_load_dword v18, v[68:69], off nt
	v_add_co_u32_e32 v8, vcc, s82, v4
	s_nop 1
	v_addc_co_u32_e32 v9, vcc, 0, v5, vcc
	v_add_co_u32_e32 v10, vcc, s83, v4
	s_nop 1
	v_addc_co_u32_e32 v11, vcc, 0, v5, vcc
	v_add_co_u32_e32 v12, vcc, s84, v4
	s_nop 1
	v_addc_co_u32_e32 v13, vcc, 0, v5, vcc
	v_add_co_u32_e32 v14, vcc, s85, v4
	s_nop 1
	v_addc_co_u32_e32 v15, vcc, 0, v5, vcc
	v_add_co_u32_e32 v66, vcc, s86, v4
	s_nop 1
	v_addc_co_u32_e32 v67, vcc, 0, v5, vcc
	v_add_co_u32_e32 v68, vcc, s87, v4
	s_nop 1
	v_addc_co_u32_e32 v69, vcc, 0, v5, vcc
	v_add_co_u32_e32 v70, vcc, s88, v4
	s_nop 1
	v_addc_co_u32_e32 v71, vcc, 0, v5, vcc
	v_add_co_u32_e32 v4, vcc, s89, v4
	s_nop 1
	v_addc_co_u32_e32 v5, vcc, 0, v5, vcc
	global_load_dword v17, v[8:9], off nt
	global_load_dword v16, v[10:11], off nt
	s_nop 0
	global_load_dword v13, v[12:13], off nt
	s_nop 0
	global_load_dword v11, v[14:15], off nt
	global_load_dword v9, v[66:67], off nt
	global_load_dword v8, v[68:69], off nt
	global_load_dword v7, v[70:71], off nt
	s_nop 0
	global_load_dword v4, v[4:5], off nt
	s_waitcnt vmcnt(62)
	s_barrier
	v_mul_f32_e32 v130, 0xbfb8aa3b, v128
	v_exp_f32_e32 v130, v130
	s_nop 0
	v_add_f32_e32 v130, 1.0, v130
	v_div_scale_f32 v131, s[94:95], v130, v130, v128
	v_rcp_f32_e32 v132, v131
	v_div_scale_f32 v133, vcc, v128, v130, v128
	v_fma_f32 v134, -v131, v132, 1.0
	v_fmac_f32_e32 v132, v134, v132
	v_mul_f32_e32 v134, v133, v132
	v_fma_f32 v135, -v131, v134, v133
	v_fmac_f32_e32 v134, v135, v132
	v_fma_f32 v131, -v131, v134, v133
	v_div_fmas_f32 v131, v131, v132, v134
	v_div_fixup_f32 v128, v131, v130, v128
	ds_write_b32 v182, v128
	s_mov_b64 s[18:19], exec
	v_cmpx_gt_u32_e32 vcc, 64, v0
	v_mul_f32_e32 v130, 0xbfb8aa3b, v129
	v_exp_f32_e32 v130, v130
	s_nop 0
	v_add_f32_e32 v130, 1.0, v130
	v_div_scale_f32 v131, s[94:95], v130, v130, v129
	v_rcp_f32_e32 v132, v131
	v_div_scale_f32 v133, vcc, v129, v130, v129
	v_fma_f32 v134, -v131, v132, 1.0
	v_fmac_f32_e32 v132, v134, v132
	v_mul_f32_e32 v134, v133, v132
	v_fma_f32 v135, -v131, v134, v133
	v_fmac_f32_e32 v134, v135, v132
	v_fma_f32 v131, -v131, v134, v133
	v_div_fmas_f32 v131, v131, v132, v134
	v_div_fixup_f32 v129, v131, v130, v129
	ds_write_b32 v182, v129 offset:1024
	s_mov_b64 exec, s[18:19]
	s_waitcnt lgkmcnt(0)
	s_barrier
	ds_read_b128 v[66:69], v6
	ds_read_b128 v[70:73], v6 offset:16
	ds_read_b128 v[74:77], v6 offset:256
	ds_read_b128 v[78:81], v6 offset:32
	ds_read_b128 v[82:85], v6 offset:48
	ds_read_b128 v[86:89], v6 offset:512
	ds_read_b128 v[90:93], v6 offset:272
	ds_read_b128 v[94:97], v6 offset:768
	ds_read_b128 v[98:101], v6 offset:1024
	ds_read_b128 v[102:105], v6 offset:528
	s_waitcnt vmcnt(62) lgkmcnt(9)
	v_fma_f32 v5, v114, v66, 0
	s_waitcnt lgkmcnt(7)
	v_fma_f32 v14, v114, v74, 0
	v_fmac_f32_e32 v5, v115, v67
	v_fmac_f32_e32 v14, v115, v75
	ds_read_b128 v[106:109], v6 offset:784
	ds_read_b128 v[110:113], v6 offset:1040
	s_waitcnt vmcnt(61)
	v_fmac_f32_e32 v5, v116, v68
	v_fmac_f32_e32 v14, v116, v76
	s_waitcnt lgkmcnt(6)
	v_fma_f32 v15, v114, v86, 0
	s_waitcnt lgkmcnt(4)
	v_fma_f32 v12, v114, v94, 0
	s_waitcnt lgkmcnt(3)
	v_fma_f32 v10, v114, v98, 0
	s_waitcnt vmcnt(60)
	v_fmac_f32_e32 v5, v117, v69
	v_fmac_f32_e32 v14, v117, v77
	v_fmac_f32_e32 v15, v115, v87
	v_fmac_f32_e32 v12, v115, v95
	v_fmac_f32_e32 v10, v115, v99
	s_waitcnt vmcnt(59)
	v_fmac_f32_e32 v5, v118, v70
	v_fmac_f32_e32 v14, v118, v90
	v_fmac_f32_e32 v15, v116, v88
	v_fmac_f32_e32 v12, v116, v96
	v_fmac_f32_e32 v10, v116, v100
	s_waitcnt vmcnt(58)
	v_fmac_f32_e32 v5, v119, v71
	v_fmac_f32_e32 v14, v119, v91
	v_fmac_f32_e32 v15, v117, v89
	v_fmac_f32_e32 v12, v117, v97
	v_fmac_f32_e32 v10, v117, v101
	s_waitcnt vmcnt(57)
	v_fmac_f32_e32 v5, v120, v72
	v_fmac_f32_e32 v14, v120, v92
	ds_read_b128 v[66:69], v6 offset:288
	s_waitcnt lgkmcnt(3)
; __device__ void adaln_partial_task(KParams& p, int task, float* sm) {
;     ...
; #pragma unroll
;     for (int k = 0; k < 64; ++k) {
;       a0 += sc[k] * wv[k]; a1 += sc[64 + k] * wv[k]; a2 += sc[128 + k] * wv[k]; a3 += sc[192 + k] * wv[k]; a4 += sc[256 + k] * wv[k];
;     }
	v_fmac_f32_e32 v15, v118, v102
	s_waitcnt lgkmcnt(2)
	v_fmac_f32_e32 v12, v118, v106
	s_waitcnt lgkmcnt(1)
	v_fmac_f32_e32 v10, v118, v110
	s_waitcnt vmcnt(56)
	v_fmac_f32_e32 v5, v121, v73
	v_fmac_f32_e32 v14, v121, v93
	ds_read_b128 v[70:73], v6 offset:544
	ds_read_b128 v[74:77], v6 offset:304
	ds_read_b128 v[86:89], v6 offset:800
	ds_read_b128 v[90:93], v6 offset:1056
	ds_read_b128 v[94:97], v6 offset:560
	v_fmac_f32_e32 v15, v119, v103
	v_fmac_f32_e32 v12, v119, v107
	v_fmac_f32_e32 v10, v119, v111
	v_fmac_f32_e32 v15, v120, v104
	v_fmac_f32_e32 v12, v120, v108
	v_fmac_f32_e32 v10, v120, v112
	v_fmac_f32_e32 v15, v121, v105
	v_fmac_f32_e32 v12, v121, v109
	v_fmac_f32_e32 v10, v121, v113
	ds_read_b128 v[98:101], v6 offset:816
	ds_read_b128 v[102:105], v6 offset:1072
	s_waitcnt vmcnt(55)
	v_fmac_f32_e32 v5, v65, v78
	s_waitcnt lgkmcnt(7)
	v_fmac_f32_e32 v14, v65, v66
	s_waitcnt lgkmcnt(6)
	v_fmac_f32_e32 v15, v65, v70
	s_waitcnt lgkmcnt(4)
	v_fmac_f32_e32 v12, v65, v86
	s_waitcnt lgkmcnt(3)
	v_fmac_f32_e32 v10, v65, v90
	s_waitcnt vmcnt(54)
	v_fmac_f32_e32 v5, v64, v79
	v_fmac_f32_e32 v14, v64, v67
	v_fmac_f32_e32 v15, v64, v71
	v_fmac_f32_e32 v12, v64, v87
	v_fmac_f32_e32 v10, v64, v91
	s_waitcnt vmcnt(53)
	v_fmac_f32_e32 v5, v63, v80
	v_fmac_f32_e32 v14, v63, v68
	v_fmac_f32_e32 v15, v63, v72
	v_fmac_f32_e32 v12, v63, v88
	v_fmac_f32_e32 v10, v63, v92
	s_waitcnt vmcnt(52)
	v_fmac_f32_e32 v5, v62, v81
	v_fmac_f32_e32 v14, v62, v69
	v_fmac_f32_e32 v15, v62, v73
	v_fmac_f32_e32 v12, v62, v89
	v_fmac_f32_e32 v10, v62, v93
	s_waitcnt vmcnt(51)
	v_fmac_f32_e32 v5, v61, v82
	v_fmac_f32_e32 v14, v61, v74
	s_waitcnt lgkmcnt(2)
	v_fmac_f32_e32 v15, v61, v94
	s_waitcnt lgkmcnt(1)
	v_fmac_f32_e32 v12, v61, v98
	s_waitcnt lgkmcnt(0)
	v_fmac_f32_e32 v10, v61, v102
	s_waitcnt vmcnt(50)
	v_fmac_f32_e32 v5, v60, v83
	v_fmac_f32_e32 v14, v60, v75
	v_fmac_f32_e32 v15, v60, v95
	v_fmac_f32_e32 v12, v60, v99
	v_fmac_f32_e32 v10, v60, v103
	ds_read_b128 v[60:63], v6 offset:64
	s_waitcnt vmcnt(49)
	v_fmac_f32_e32 v5, v59, v84
	v_fmac_f32_e32 v14, v59, v76
	ds_read_b128 v[64:67], v6 offset:320
	ds_read_b128 v[68:71], v6 offset:80
	s_waitcnt vmcnt(48)
	v_fmac_f32_e32 v5, v58, v85
	v_fmac_f32_e32 v14, v58, v77
	ds_read_b128 v[72:75], v6 offset:576
	ds_read_b128 v[76:79], v6 offset:336
	ds_read_b128 v[80:83], v6 offset:832
	ds_read_b128 v[84:87], v6 offset:1088
	ds_read_b128 v[88:91], v6 offset:592
	v_fmac_f32_e32 v15, v59, v96
	v_fmac_f32_e32 v12, v59, v100
	v_fmac_f32_e32 v10, v59, v104
	v_fmac_f32_e32 v15, v58, v97
	v_fmac_f32_e32 v12, v58, v101
	v_fmac_f32_e32 v10, v58, v105
	s_waitcnt vmcnt(47) lgkmcnt(7)
	v_fmac_f32_e32 v5, v57, v60
	s_waitcnt lgkmcnt(6)
	v_fmac_f32_e32 v14, v57, v64
	ds_read_b128 v[92:95], v6 offset:848
	ds_read_b128 v[96:99], v6 offset:1104
	s_waitcnt lgkmcnt(6)
	v_fmac_f32_e32 v15, v57, v72
	s_waitcnt lgkmcnt(4)
	v_fmac_f32_e32 v12, v57, v80
	s_waitcnt lgkmcnt(3)
	v_fmac_f32_e32 v10, v57, v84
	s_waitcnt vmcnt(46)
	v_fmac_f32_e32 v5, v56, v61
	v_fmac_f32_e32 v14, v56, v65
	v_fmac_f32_e32 v15, v56, v73
	v_fmac_f32_e32 v12, v56, v81
	v_fmac_f32_e32 v10, v56, v85
	s_waitcnt vmcnt(45)
	v_fmac_f32_e32 v5, v55, v62
	v_fmac_f32_e32 v14, v55, v66
	v_fmac_f32_e32 v15, v55, v74
	v_fmac_f32_e32 v12, v55, v82
	v_fmac_f32_e32 v10, v55, v86
	s_waitcnt vmcnt(44)
	v_fmac_f32_e32 v5, v54, v63
	v_fmac_f32_e32 v14, v54, v67
	v_fmac_f32_e32 v15, v54, v75
	v_fmac_f32_e32 v12, v54, v83
	v_fmac_f32_e32 v10, v54, v87
	s_waitcnt vmcnt(43)
	v_fmac_f32_e32 v5, v53, v68
	v_fmac_f32_e32 v14, v53, v76
	s_waitcnt lgkmcnt(2)
	v_fmac_f32_e32 v15, v53, v88
	s_waitcnt lgkmcnt(1)
	v_fmac_f32_e32 v12, v53, v92
	s_waitcnt lgkmcnt(0)
	v_fmac_f32_e32 v10, v53, v96
	s_waitcnt vmcnt(42)
	v_fmac_f32_e32 v5, v52, v69
	v_fmac_f32_e32 v14, v52, v77
	v_fmac_f32_e32 v15, v52, v89
	v_fmac_f32_e32 v12, v52, v93
	v_fmac_f32_e32 v10, v52, v97
	s_waitcnt vmcnt(41)
	v_fmac_f32_e32 v5, v51, v70
	v_fmac_f32_e32 v14, v51, v78
	ds_read_b128 v[52:55], v6 offset:96
	s_waitcnt vmcnt(40)
	v_fmac_f32_e32 v5, v50, v71
	v_fmac_f32_e32 v14, v50, v79
	ds_read_b128 v[56:59], v6 offset:352
	ds_read_b128 v[60:63], v6 offset:112
	ds_read_b128 v[64:67], v6 offset:608
	ds_read_b128 v[68:71], v6 offset:368
	ds_read_b128 v[72:75], v6 offset:864
	ds_read_b128 v[76:79], v6 offset:1120
	ds_read_b128 v[80:83], v6 offset:624
	v_fmac_f32_e32 v15, v51, v90
	v_fmac_f32_e32 v12, v51, v94
	v_fmac_f32_e32 v10, v51, v98
	v_fmac_f32_e32 v15, v50, v91
	v_fmac_f32_e32 v12, v50, v95
	v_fmac_f32_e32 v10, v50, v99
	ds_read_b128 v[84:87], v6 offset:880
	ds_read_b128 v[88:91], v6 offset:1136
	s_waitcnt vmcnt(39) lgkmcnt(9)
	v_fmac_f32_e32 v5, v49, v52
	s_waitcnt lgkmcnt(8)
	v_fmac_f32_e32 v14, v49, v56
	s_waitcnt lgkmcnt(6)
	v_fmac_f32_e32 v15, v49, v64
	s_waitcnt lgkmcnt(4)
	v_fmac_f32_e32 v12, v49, v72
	s_waitcnt lgkmcnt(3)
	v_fmac_f32_e32 v10, v49, v76
	s_waitcnt vmcnt(38)
	v_fmac_f32_e32 v5, v48, v53
	v_fmac_f32_e32 v14, v48, v57
	v_fmac_f32_e32 v15, v48, v65
	v_fmac_f32_e32 v12, v48, v73
	v_fmac_f32_e32 v10, v48, v77
	s_waitcnt vmcnt(37)
	v_fmac_f32_e32 v5, v47, v54
	v_fmac_f32_e32 v14, v47, v58
	v_fmac_f32_e32 v15, v47, v66
	v_fmac_f32_e32 v12, v47, v74
	v_fmac_f32_e32 v10, v47, v78
	s_waitcnt vmcnt(36)
	v_fmac_f32_e32 v5, v46, v55
	v_fmac_f32_e32 v14, v46, v59
	v_fmac_f32_e32 v15, v46, v67
	v_fmac_f32_e32 v12, v46, v75
	v_fmac_f32_e32 v10, v46, v79
	s_waitcnt vmcnt(35)
	v_fmac_f32_e32 v5, v45, v60
	v_fmac_f32_e32 v14, v45, v68
	s_waitcnt lgkmcnt(2)
	v_fmac_f32_e32 v15, v45, v80
	s_waitcnt lgkmcnt(1)
	v_fmac_f32_e32 v12, v45, v84
	s_waitcnt lgkmcnt(0)
	v_fmac_f32_e32 v10, v45, v88
	s_waitcnt vmcnt(34)
; __device__ void adaln_partial_task(KParams& p, int task, float* sm) {
;     ...
; #pragma unroll
;     for (int k = 0; k < 64; ++k) {
;       a0 += sc[k] * wv[k]; a1 += sc[64 + k] * wv[k]; a2 += sc[128 + k] * wv[k]; a3 += sc[192 + k] * wv[k]; a4 += sc[256 + k] * wv[k];
;     }
	v_fmac_f32_e32 v5, v44, v61
	v_fmac_f32_e32 v14, v44, v69
	v_fmac_f32_e32 v15, v44, v81
	v_fmac_f32_e32 v12, v44, v85
	v_fmac_f32_e32 v10, v44, v89
	ds_read_b128 v[44:47], v6 offset:128
	s_waitcnt vmcnt(33)
	v_fmac_f32_e32 v5, v43, v62
	v_fmac_f32_e32 v14, v43, v70
	ds_read_b128 v[48:51], v6 offset:384
	ds_read_b128 v[52:55], v6 offset:144
	s_waitcnt vmcnt(32)
	v_fmac_f32_e32 v5, v42, v63
	v_fmac_f32_e32 v14, v42, v71
	ds_read_b128 v[56:59], v6 offset:640
	ds_read_b128 v[60:63], v6 offset:400
	ds_read_b128 v[64:67], v6 offset:896
	ds_read_b128 v[68:71], v6 offset:1152
	ds_read_b128 v[72:75], v6 offset:656
	v_fmac_f32_e32 v15, v43, v82
	v_fmac_f32_e32 v12, v43, v86
	v_fmac_f32_e32 v10, v43, v90
	v_fmac_f32_e32 v15, v42, v83
	v_fmac_f32_e32 v12, v42, v87
	v_fmac_f32_e32 v10, v42, v91
	s_waitcnt vmcnt(31) lgkmcnt(7)
	v_fmac_f32_e32 v5, v41, v44
	s_waitcnt lgkmcnt(6)
	v_fmac_f32_e32 v14, v41, v48
	ds_read_b128 v[76:79], v6 offset:912
	ds_read_b128 v[80:83], v6 offset:1168
	s_waitcnt lgkmcnt(6)
	v_fmac_f32_e32 v15, v41, v56
	s_waitcnt lgkmcnt(4)
	v_fmac_f32_e32 v12, v41, v64
	s_waitcnt lgkmcnt(3)
	v_fmac_f32_e32 v10, v41, v68
	s_waitcnt vmcnt(30)
	v_fmac_f32_e32 v5, v40, v45
	v_fmac_f32_e32 v14, v40, v49
	v_fmac_f32_e32 v15, v40, v57
	v_fmac_f32_e32 v12, v40, v65
	v_fmac_f32_e32 v10, v40, v69
	s_waitcnt vmcnt(29)
	v_fmac_f32_e32 v5, v39, v46
	v_fmac_f32_e32 v14, v39, v50
	v_fmac_f32_e32 v15, v39, v58
	v_fmac_f32_e32 v12, v39, v66
	v_fmac_f32_e32 v10, v39, v70
	s_waitcnt vmcnt(28)
	v_fmac_f32_e32 v5, v38, v47
	v_fmac_f32_e32 v14, v38, v51
	v_fmac_f32_e32 v15, v38, v59
	v_fmac_f32_e32 v12, v38, v67
	v_fmac_f32_e32 v10, v38, v71
	s_waitcnt vmcnt(27)
	v_fmac_f32_e32 v5, v37, v52
	v_fmac_f32_e32 v14, v37, v60
	s_waitcnt lgkmcnt(2)
	v_fmac_f32_e32 v15, v37, v72
	s_waitcnt lgkmcnt(1)
	v_fmac_f32_e32 v12, v37, v76
	s_waitcnt lgkmcnt(0)
	v_fmac_f32_e32 v10, v37, v80
	s_waitcnt vmcnt(26)
	v_fmac_f32_e32 v5, v36, v53
	v_fmac_f32_e32 v14, v36, v61
	v_fmac_f32_e32 v15, v36, v73
	v_fmac_f32_e32 v12, v36, v77
	v_fmac_f32_e32 v10, v36, v81
	s_waitcnt vmcnt(25)
	v_fmac_f32_e32 v5, v35, v54
	v_fmac_f32_e32 v14, v35, v62
	ds_read_b128 v[36:39], v6 offset:160
	s_waitcnt vmcnt(24)
	v_fmac_f32_e32 v5, v34, v55
	v_fmac_f32_e32 v14, v34, v63
	ds_read_b128 v[40:43], v6 offset:416
	ds_read_b128 v[44:47], v6 offset:176
	ds_read_b128 v[48:51], v6 offset:672
	ds_read_b128 v[52:55], v6 offset:432
	ds_read_b128 v[56:59], v6 offset:928
	ds_read_b128 v[60:63], v6 offset:1184
	ds_read_b128 v[64:67], v6 offset:688
	v_fmac_f32_e32 v15, v35, v74
	v_fmac_f32_e32 v12, v35, v78
	v_fmac_f32_e32 v10, v35, v82
	v_fmac_f32_e32 v15, v34, v75
	v_fmac_f32_e32 v12, v34, v79
	v_fmac_f32_e32 v10, v34, v83
	ds_read_b128 v[68:71], v6 offset:944
	ds_read_b128 v[72:75], v6 offset:1200
	s_waitcnt vmcnt(23) lgkmcnt(9)
	v_fmac_f32_e32 v5, v33, v36
	s_waitcnt lgkmcnt(8)
	v_fmac_f32_e32 v14, v33, v40
	s_waitcnt lgkmcnt(6)
	v_fmac_f32_e32 v15, v33, v48
	s_waitcnt lgkmcnt(4)
	v_fmac_f32_e32 v12, v33, v56
	s_waitcnt lgkmcnt(3)
	v_fmac_f32_e32 v10, v33, v60
	s_waitcnt vmcnt(22)
	v_fmac_f32_e32 v5, v32, v37
	v_fmac_f32_e32 v14, v32, v41
	v_fmac_f32_e32 v15, v32, v49
	v_fmac_f32_e32 v12, v32, v57
	v_fmac_f32_e32 v10, v32, v61
	s_waitcnt vmcnt(21)
	v_fmac_f32_e32 v5, v31, v38
	v_fmac_f32_e32 v14, v31, v42
	v_fmac_f32_e32 v15, v31, v50
	v_fmac_f32_e32 v12, v31, v58
	v_fmac_f32_e32 v10, v31, v62
	s_waitcnt vmcnt(20)
	v_fmac_f32_e32 v5, v30, v39
	v_fmac_f32_e32 v14, v30, v43
	v_fmac_f32_e32 v15, v30, v51
	v_fmac_f32_e32 v12, v30, v59
	v_fmac_f32_e32 v10, v30, v63
	s_waitcnt vmcnt(19)
	v_fmac_f32_e32 v5, v29, v44
	v_fmac_f32_e32 v14, v29, v52
	s_waitcnt lgkmcnt(2)
	v_fmac_f32_e32 v15, v29, v64
	s_waitcnt lgkmcnt(1)
	v_fmac_f32_e32 v12, v29, v68
	s_waitcnt lgkmcnt(0)
	v_fmac_f32_e32 v10, v29, v72
	s_waitcnt vmcnt(18)
	v_fmac_f32_e32 v5, v28, v45
	v_fmac_f32_e32 v14, v28, v53
	v_fmac_f32_e32 v15, v28, v65
	v_fmac_f32_e32 v12, v28, v69
	v_fmac_f32_e32 v10, v28, v73
	ds_read_b128 v[28:31], v6 offset:192
	s_waitcnt vmcnt(17)
	v_fmac_f32_e32 v5, v27, v46
	v_fmac_f32_e32 v14, v27, v54
	ds_read_b128 v[32:35], v6 offset:448
	ds_read_b128 v[36:39], v6 offset:208
	s_waitcnt vmcnt(16)
	v_fmac_f32_e32 v5, v26, v47
	v_fmac_f32_e32 v14, v26, v55
	ds_read_b128 v[40:43], v6 offset:704
	ds_read_b128 v[44:47], v6 offset:464
	ds_read_b128 v[48:51], v6 offset:960
	ds_read_b128 v[52:55], v6 offset:1216
	ds_read_b128 v[56:59], v6 offset:720
	v_fmac_f32_e32 v15, v27, v66
	v_fmac_f32_e32 v12, v27, v70
	v_fmac_f32_e32 v10, v27, v74
	v_fmac_f32_e32 v15, v26, v67
	v_fmac_f32_e32 v12, v26, v71
	v_fmac_f32_e32 v10, v26, v75
	s_waitcnt vmcnt(15) lgkmcnt(7)
; __device__ __forceinline__ float silu_f(float v) { return v / (1.f + __expf(-v)); }
; __device__ void adaln_partial_task(KParams& p, int task, float* sm) {
;   const int cb = task % 48, ks = task / 48, tid = threadIdx.x;
;   float* sc = sm;
;   __syncthreads();
;   for (int i = tid; i < 5 * 64; i += NTHREADS) {
;     int r = i >> 6, kk = i & 63;
;     int k = ks * 64 + kk;
;     float cv = (r < 4) ? p.c[r * D + k] : p.c_ctx[k];
;     sc[i] = silu_f(cv);
;   }
;   __syncthreads();
;     ...
; #pragma unroll
;     for (int k = 0; k < 64; ++k) {
;       a0 += sc[k] * wv[k]; a1 += sc[64 + k] * wv[k]; a2 += sc[128 + k] * wv[k]; a3 += sc[192 + k] * wv[k]; a4 += sc[256 + k] * wv[k];
;     }
;   }
;   float* pp = p.partial + (size_t)ks * 5 * NMOD + col;
;   pp[0] = a0; pp[NMOD] = a1; pp[2 * NMOD] = a2; pp[3 * NMOD] = a3; pp[4 * NMOD] = a4;
	v_fmac_f32_e32 v5, v25, v28
	s_waitcnt lgkmcnt(6)
	v_fmac_f32_e32 v14, v25, v32
	ds_read_b128 v[60:63], v6 offset:976
	ds_read_b128 v[64:67], v6 offset:1232
	s_waitcnt lgkmcnt(6)
	v_fmac_f32_e32 v15, v25, v40
	s_waitcnt lgkmcnt(4)
	v_fmac_f32_e32 v12, v25, v48
	s_waitcnt lgkmcnt(3)
	v_fmac_f32_e32 v10, v25, v52
	s_waitcnt vmcnt(14)
	v_fmac_f32_e32 v5, v24, v29
	v_fmac_f32_e32 v14, v24, v33
	v_fmac_f32_e32 v15, v24, v41
	v_fmac_f32_e32 v12, v24, v49
	v_fmac_f32_e32 v10, v24, v53
	s_waitcnt vmcnt(13)
	v_fmac_f32_e32 v5, v23, v30
	v_fmac_f32_e32 v14, v23, v34
	v_fmac_f32_e32 v15, v23, v42
	v_fmac_f32_e32 v12, v23, v50
	v_fmac_f32_e32 v10, v23, v54
	s_waitcnt vmcnt(12)
	v_fmac_f32_e32 v5, v22, v31
	v_fmac_f32_e32 v14, v22, v35
	v_fmac_f32_e32 v15, v22, v43
	v_fmac_f32_e32 v12, v22, v51
	v_fmac_f32_e32 v10, v22, v55
	s_waitcnt vmcnt(11)
	v_fmac_f32_e32 v5, v21, v36
	v_fmac_f32_e32 v14, v21, v44
	s_waitcnt lgkmcnt(2)
	v_fmac_f32_e32 v15, v21, v56
	s_waitcnt lgkmcnt(1)
	v_fmac_f32_e32 v12, v21, v60
	s_waitcnt lgkmcnt(0)
	v_fmac_f32_e32 v10, v21, v64
	s_waitcnt vmcnt(10)
	v_fmac_f32_e32 v5, v20, v37
	v_fmac_f32_e32 v14, v20, v45
	v_fmac_f32_e32 v15, v20, v57
	v_fmac_f32_e32 v12, v20, v61
	v_fmac_f32_e32 v10, v20, v65
	s_waitcnt vmcnt(9)
	v_fmac_f32_e32 v5, v19, v38
	v_fmac_f32_e32 v14, v19, v46
	ds_read_b128 v[20:23], v6 offset:224
	s_waitcnt vmcnt(8)
	v_fmac_f32_e32 v5, v18, v39
	v_fmac_f32_e32 v14, v18, v47
	ds_read_b128 v[24:27], v6 offset:480
	ds_read_b128 v[28:31], v6 offset:240
	ds_read_b128 v[32:35], v6 offset:736
	ds_read_b128 v[36:39], v6 offset:496
	ds_read_b128 v[40:43], v6 offset:992
	ds_read_b128 v[44:47], v6 offset:1248
	ds_read_b128 v[48:51], v6 offset:752
	v_fmac_f32_e32 v15, v19, v58
	v_fmac_f32_e32 v12, v19, v62
	v_fmac_f32_e32 v10, v19, v66
	v_fmac_f32_e32 v15, v18, v59
	v_fmac_f32_e32 v12, v18, v63
	v_fmac_f32_e32 v10, v18, v67
	ds_read_b128 v[52:55], v6 offset:1008
	ds_read_b128 v[56:59], v6 offset:1264
	s_waitcnt vmcnt(7) lgkmcnt(9)
	v_fmac_f32_e32 v5, v17, v20
	s_waitcnt lgkmcnt(8)
	v_fmac_f32_e32 v14, v17, v24
	s_waitcnt lgkmcnt(6)
	v_fmac_f32_e32 v15, v17, v32
	s_waitcnt lgkmcnt(4)
	v_fmac_f32_e32 v12, v17, v40
	s_waitcnt lgkmcnt(3)
	v_fmac_f32_e32 v10, v17, v44
	s_waitcnt vmcnt(6)
	v_fmac_f32_e32 v5, v16, v21
	v_fmac_f32_e32 v14, v16, v25
	v_fmac_f32_e32 v15, v16, v33
	v_fmac_f32_e32 v12, v16, v41
	v_fmac_f32_e32 v10, v16, v45
	s_waitcnt vmcnt(5)
	v_fmac_f32_e32 v5, v13, v22
	v_fmac_f32_e32 v14, v13, v26
	v_fmac_f32_e32 v15, v13, v34
	v_fmac_f32_e32 v12, v13, v42
	v_fmac_f32_e32 v10, v13, v46
	s_waitcnt vmcnt(4)
	v_fmac_f32_e32 v5, v11, v23
	v_fmac_f32_e32 v14, v11, v27
	v_fmac_f32_e32 v15, v11, v35
	v_fmac_f32_e32 v12, v11, v43
	v_fmac_f32_e32 v10, v11, v47
	s_waitcnt vmcnt(3)
	v_fmac_f32_e32 v5, v9, v28
	v_fmac_f32_e32 v14, v9, v36
	s_waitcnt lgkmcnt(2)
	v_fmac_f32_e32 v15, v9, v48
	s_waitcnt lgkmcnt(1)
	v_fmac_f32_e32 v12, v9, v52
	s_waitcnt lgkmcnt(0)
	v_fmac_f32_e32 v10, v9, v56
	s_waitcnt vmcnt(2)
	v_fmac_f32_e32 v5, v8, v29
	v_fmac_f32_e32 v14, v8, v37
	v_fmac_f32_e32 v15, v8, v49
	v_fmac_f32_e32 v12, v8, v53
	v_fmac_f32_e32 v10, v8, v57
	s_waitcnt vmcnt(1)
	v_fmac_f32_e32 v5, v7, v30
	v_fmac_f32_e32 v14, v7, v38
	v_fmac_f32_e32 v15, v7, v50
	v_fmac_f32_e32 v12, v7, v54
	v_fmac_f32_e32 v10, v7, v58
	s_waitcnt vmcnt(0)
	v_fmac_f32_e32 v5, v4, v31
	v_fmac_f32_e32 v14, v4, v39
	v_fmac_f32_e32 v15, v4, v51
	v_fmac_f32_e32 v12, v4, v55
	v_fmac_f32_e32 v10, v4, v59
	v_add_co_u32_e32 v4, vcc, s22, v2
	global_store_dword v[2:3], v5, off
	s_nop 0
	v_addc_co_u32_e32 v5, vcc, 0, v3, vcc
	global_store_dword v[4:5], v14, off
	v_add_co_u32_e32 v4, vcc, 0x18000, v2
	s_nop 1
	v_addc_co_u32_e32 v5, vcc, 0, v3, vcc
	global_store_dword v[4:5], v15, off
	v_add_co_u32_e32 v4, vcc, 0x24000, v2
	s_nop 1
	v_addc_co_u32_e32 v5, vcc, 0, v3, vcc
	v_add_co_u32_e32 v2, vcc, 0x30000, v2
	global_store_dword v[4:5], v12, off
	s_nop 0
	v_addc_co_u32_e32 v3, vcc, 0, v3, vcc
	global_store_dword v[2:3], v10, off
	s_cbranch_scc1 .LBB0_19
.LBB0_16:
	s_mul_hi_i32 s18, s90, 0x2aaaaaab
	s_lshr_b32 s19, s18, 31
	s_ashr_i32 s91, s18, 3
	s_add_i32 s91, s91, s19
	s_lshl_b32 s92, s91, 6
	s_waitcnt lgkmcnt(0)
	v_or_b32_e32 v122, s92, v184
	v_ashrrev_i32_e32 v123, 31, v122
	v_lshl_add_u64 v[124:125], v[122:123], 2, s[8:9]
	v_lshlrev_b32_e32 v126, 5, v0
	v_and_b32_e32 v126, 0x1800, v126
	v_add_u32_e32 v126, v126, v122
	v_ashrrev_i32_e32 v127, 31, v126
	v_lshl_add_u64 v[126:127], v[126:127], 2, s[14:15]
	global_load_dword v128, v[126:127], off
	v_cmp_gt_u32_e32 vcc, 64, v0
	s_and_saveexec_b64 s[18:19], vcc
	global_load_dword v129, v[124:125], off
	s_branch .LBB0_15
